# v61 + nt on the P7 gate loads (mid-K fold and epilogue reads of the cold ZG columns)
# baseline (speedup 1.0000x reference)
; __device__ __forceinline__ int fresh_lane() { int l; asm volatile("v_mbcnt_lo_u32_b32 %0, -1, 0\n\tv_mbcnt_hi_u32_b32 %0, -1, %0" : "=v"(l)); return l; }
; __device__ __forceinline__ float bf_lo(unsigned w) { return __uint_as_float(w << 16); }
; __device__ __forceinline__ float bf_hi(unsigned w) { return __uint_as_float(w & 0xffff0000u); }
;     __device__ __forceinline__ void mid(f32x4 (&acc)[2][2][4][2], const Unit& u, int wr, int wc) const {
;         const int l_ = fresh_lane(), fr = l_ & 15, fq = l_ >> 4;
;         const int row0 = u.pm * BM + wr * 64 + fr, col0 = u.pn * BM + wc * 32 + 4 * fq;
; #pragma unroll
;         for (int ai = 0; ai < 2; ++ai)
; #pragma unroll
;             for (int m = 0; m < 4; ++m) { const size_t r = (size_t)(row0 + ai * HALF + m * 16);
; #pragma unroll
;                 for (int bj = 0; bj < 2; ++bj)
; #pragma unroll
;                     for (int n = 0; n < 2; ++n) { const u32x2 ga = *(const u32x2*)(G + r * ldg + col0 + bj * HALF + n * 16), gb = *(const u32x2*)(G + r * ldg + 4096 + col0 + bj * HALF + n * 16); f32x4 a = acc[ai][bj][m][n];
;                         a[0] *= bf_lo(ga.x) * __builtin_amdgcn_rcpf(bf_lo(gb.x)); a[1] *= bf_hi(ga.x) * __builtin_amdgcn_rcpf(bf_hi(gb.x)); a[2] *= bf_lo(ga.y) * __builtin_amdgcn_rcpf(bf_lo(gb.y)); a[3] *= bf_hi(ga.y) * __builtin_amdgcn_rcpf(bf_hi(gb.y));
;                         acc[ai][bj][m][n] = a; }
;                 asm volatile("" ::: "memory"); }
.LBB0_2990:
	s_cmpk_lg_i32 s52, 0x800
	s_cbranch_scc1 .LBB0_2989
	v_mbcnt_lo_u32_b32 v135, -1, 0
	v_mbcnt_hi_u32_b32 v135, -1, v135
	s_mov_b64 s[54:55], 0x200000
	v_ashrrev_i32_e32 v134, 2, v135
	v_and_or_b32 v135, v135, 15, s74
	v_and_b32_e32 v134, -4, v134
	v_add_u32_e32 v142, s87, v135
	v_add_u32_e32 v134, s43, v134
	v_ashrrev_i32_e32 v143, 31, v142
	v_ashrrev_i32_e32 v135, 31, v134
	v_lshlrev_b64 v[136:137], 14, v[142:143]
	v_lshl_add_u64 v[136:137], s[12:13], 0, v[136:137]
	v_lshlrev_b64 v[144:145], 1, v[134:135]
	v_lshl_add_u64 v[140:141], v[136:137], 0, v[144:145]
	v_add_co_u32_e32 v146, vcc, s66, v140
	global_load_dwordx2 v[134:135], v[140:141], off nt
	s_nop 0
	v_addc_co_u32_e32 v147, vcc, 0, v141, vcc
	global_load_dwordx2 v[136:137], v[146:147], off nt
	s_waitcnt vmcnt(0)
	v_lshlrev_b32_e32 v152, 16, v134
	v_and_b32_e32 v153, 0xffff0000, v134
	v_lshlrev_b32_e32 v143, 16, v136
	v_and_b32_e32 v136, 0xffff0000, v136
	v_lshlrev_b32_e32 v134, 16, v137
	v_rcp_f32_e32 v149, v136
	v_rcp_f32_e32 v136, v134
	v_and_b32_e32 v134, 0xffff0000, v137
	v_rcp_f32_e32 v137, v134
	v_lshlrev_b32_e32 v134, 16, v135
	v_and_b32_e32 v135, 0xffff0000, v135
	v_rcp_f32_e32 v148, v143
	v_pk_mul_f32 v[134:135], v[136:137], v[134:135]
	v_pk_mul_f32 v[148:149], v[148:149], v[152:153]
	v_pk_mul_f32 v[128:129], v[128:129], v[134:135]
	global_load_dwordx2 v[134:135], v[140:141], off offset:32 nt
	global_load_dwordx2 v[136:137], v[146:147], off offset:32 nt
	v_pk_mul_f32 v[126:127], v[126:127], v[148:149]
	s_waitcnt vmcnt(0)
	v_lshlrev_b32_e32 v152, 16, v134
	v_lshlrev_b32_e32 v143, 16, v136
	v_and_b32_e32 v136, 0xffff0000, v136
	v_and_b32_e32 v153, 0xffff0000, v134
	v_lshlrev_b32_e32 v134, 16, v137
	v_rcp_f32_e32 v149, v136
	v_rcp_f32_e32 v136, v134
	v_and_b32_e32 v134, 0xffff0000, v137
	v_rcp_f32_e32 v137, v134
	v_lshlrev_b32_e32 v134, 16, v135
	v_and_b32_e32 v135, 0xffff0000, v135
	v_rcp_f32_e32 v148, v143
	v_pk_mul_f32 v[134:135], v[136:137], v[134:135]
	v_pk_mul_f32 v[148:149], v[148:149], v[152:153]
	v_pk_mul_f32 v[124:125], v[124:125], v[134:135]
	global_load_dwordx2 v[134:135], v[140:141], off offset:256 nt
	global_load_dwordx2 v[136:137], v[146:147], off offset:256 nt
	v_pk_mul_f32 v[122:123], v[122:123], v[148:149]
	s_waitcnt vmcnt(0)
	v_lshlrev_b32_e32 v152, 16, v134
	v_lshlrev_b32_e32 v143, 16, v136
	v_and_b32_e32 v136, 0xffff0000, v136
	v_and_b32_e32 v153, 0xffff0000, v134
	v_lshlrev_b32_e32 v134, 16, v137
	v_rcp_f32_e32 v149, v136
	v_rcp_f32_e32 v136, v134
	v_and_b32_e32 v134, 0xffff0000, v137
	v_rcp_f32_e32 v137, v134
	v_lshlrev_b32_e32 v134, 16, v135
	v_and_b32_e32 v135, 0xffff0000, v135
	v_rcp_f32_e32 v148, v143
	v_pk_mul_f32 v[134:135], v[136:137], v[134:135]
	v_pk_mul_f32 v[148:149], v[148:149], v[152:153]
	v_pk_mul_f32 v[120:121], v[120:121], v[134:135]
	global_load_dwordx2 v[134:135], v[140:141], off offset:288 nt
	global_load_dwordx2 v[136:137], v[146:147], off offset:288 nt
	v_pk_mul_f32 v[118:119], v[118:119], v[148:149]
	s_waitcnt vmcnt(0)
	v_lshlrev_b32_e32 v148, 16, v134
	v_lshlrev_b32_e32 v143, 16, v136
	v_and_b32_e32 v136, 0xffff0000, v136
	v_and_b32_e32 v149, 0xffff0000, v134
	v_lshlrev_b32_e32 v134, 16, v137
	v_rcp_f32_e32 v147, v136
	v_rcp_f32_e32 v136, v134
	v_and_b32_e32 v134, 0xffff0000, v137
	v_rcp_f32_e32 v137, v134
	v_lshlrev_b32_e32 v134, 16, v135
	v_and_b32_e32 v135, 0xffff0000, v135
	v_rcp_f32_e32 v146, v143
	v_pk_mul_f32 v[134:135], v[136:137], v[134:135]
	v_pk_mul_f32 v[146:147], v[146:147], v[148:149]
	v_pk_mul_f32 v[116:117], v[116:117], v[134:135]
	v_or_b32_e32 v134, 16, v142
	v_ashrrev_i32_e32 v135, 31, v134
	v_lshlrev_b64 v[134:135], 14, v[134:135]
	v_lshl_add_u64 v[134:135], s[12:13], 0, v[134:135]
	v_lshl_add_u64 v[134:135], v[134:135], 0, v[144:145]
	v_pk_mul_f32 v[114:115], v[114:115], v[146:147]
	v_add_co_u32_e32 v146, vcc, s66, v134
	global_load_dwordx2 v[136:137], v[134:135], off nt
	s_nop 0
	v_addc_co_u32_e32 v147, vcc, 0, v135, vcc
	global_load_dwordx2 v[148:149], v[146:147], off nt
	s_waitcnt vmcnt(0)
	v_lshlrev_b32_e32 v154, 16, v136
	v_and_b32_e32 v155, 0xffff0000, v136
	v_lshlrev_b32_e32 v143, 16, v148
	v_lshlrev_b32_e32 v136, 16, v149
	v_rcp_f32_e32 v152, v143
	v_and_b32_e32 v143, 0xffff0000, v148
	v_rcp_f32_e32 v148, v136
	v_and_b32_e32 v136, 0xffff0000, v149
	v_rcp_f32_e32 v149, v136
	v_lshlrev_b32_e32 v136, 16, v137
	v_and_b32_e32 v137, 0xffff0000, v137
	v_rcp_f32_e32 v153, v143
	v_pk_mul_f32 v[136:137], v[148:149], v[136:137]
	v_pk_mul_f32 v[152:153], v[152:153], v[154:155]
	v_pk_mul_f32 v[112:113], v[112:113], v[136:137]
	global_load_dwordx2 v[136:137], v[134:135], off offset:32 nt
	global_load_dwordx2 v[148:149], v[146:147], off offset:32 nt
	v_pk_mul_f32 v[110:111], v[110:111], v[152:153]
	s_waitcnt vmcnt(0)
	v_lshlrev_b32_e32 v154, 16, v136
	v_lshlrev_b32_e32 v143, 16, v148
	v_and_b32_e32 v155, 0xffff0000, v136
	v_lshlrev_b32_e32 v136, 16, v149
	v_rcp_f32_e32 v152, v143
	v_and_b32_e32 v143, 0xffff0000, v148
	v_rcp_f32_e32 v148, v136
	v_and_b32_e32 v136, 0xffff0000, v149
	v_rcp_f32_e32 v149, v136
	v_lshlrev_b32_e32 v136, 16, v137
	v_and_b32_e32 v137, 0xffff0000, v137
	v_rcp_f32_e32 v153, v143
	v_pk_mul_f32 v[136:137], v[148:149], v[136:137]
	v_pk_mul_f32 v[152:153], v[152:153], v[154:155]
	v_pk_mul_f32 v[108:109], v[108:109], v[136:137]
	global_load_dwordx2 v[136:137], v[134:135], off offset:256 nt
	global_load_dwordx2 v[148:149], v[146:147], off offset:256 nt
	v_pk_mul_f32 v[106:107], v[106:107], v[152:153]
	s_waitcnt vmcnt(0)
; __device__ __forceinline__ int fresh_lane() { int l; asm volatile("v_mbcnt_lo_u32_b32 %0, -1, 0\n\tv_mbcnt_hi_u32_b32 %0, -1, %0" : "=v"(l)); return l; }
; __device__ __forceinline__ float bf_lo(unsigned w) { return __uint_as_float(w << 16); }
; __device__ __forceinline__ float bf_hi(unsigned w) { return __uint_as_float(w & 0xffff0000u); }
;     __device__ __forceinline__ void mid(f32x4 (&acc)[2][2][4][2], const Unit& u, int wr, int wc) const {
;         const int l_ = fresh_lane(), fr = l_ & 15, fq = l_ >> 4;
;         const int row0 = u.pm * BM + wr * 64 + fr, col0 = u.pn * BM + wc * 32 + 4 * fq;
; #pragma unroll
;         for (int ai = 0; ai < 2; ++ai)
; #pragma unroll
;             for (int m = 0; m < 4; ++m) { const size_t r = (size_t)(row0 + ai * HALF + m * 16);
; #pragma unroll
;                 for (int bj = 0; bj < 2; ++bj)
; #pragma unroll
;                     for (int n = 0; n < 2; ++n) { const u32x2 ga = *(const u32x2*)(G + r * ldg + col0 + bj * HALF + n * 16), gb = *(const u32x2*)(G + r * ldg + 4096 + col0 + bj * HALF + n * 16); f32x4 a = acc[ai][bj][m][n];
;                         a[0] *= bf_lo(ga.x) * __builtin_amdgcn_rcpf(bf_lo(gb.x)); a[1] *= bf_hi(ga.x) * __builtin_amdgcn_rcpf(bf_hi(gb.x)); a[2] *= bf_lo(ga.y) * __builtin_amdgcn_rcpf(bf_lo(gb.y)); a[3] *= bf_hi(ga.y) * __builtin_amdgcn_rcpf(bf_hi(gb.y));
;                         acc[ai][bj][m][n] = a; }
;                 asm volatile("" ::: "memory"); }
	v_lshlrev_b32_e32 v154, 16, v136
	v_lshlrev_b32_e32 v143, 16, v148
	v_and_b32_e32 v155, 0xffff0000, v136
	v_lshlrev_b32_e32 v136, 16, v149
	v_rcp_f32_e32 v152, v143
	v_and_b32_e32 v143, 0xffff0000, v148
	v_rcp_f32_e32 v148, v136
	v_and_b32_e32 v136, 0xffff0000, v149
	v_rcp_f32_e32 v149, v136
	v_lshlrev_b32_e32 v136, 16, v137
	v_and_b32_e32 v137, 0xffff0000, v137
	v_rcp_f32_e32 v153, v143
	v_pk_mul_f32 v[136:137], v[148:149], v[136:137]
	v_pk_mul_f32 v[152:153], v[152:153], v[154:155]
	v_pk_mul_f32 v[104:105], v[104:105], v[136:137]
	global_load_dwordx2 v[134:135], v[134:135], off offset:288 nt
	s_nop 0
	global_load_dwordx2 v[136:137], v[146:147], off offset:288 nt
	v_pk_mul_f32 v[102:103], v[102:103], v[152:153]
	s_waitcnt vmcnt(0)
	v_lshlrev_b32_e32 v148, 16, v134
	v_lshlrev_b32_e32 v143, 16, v136
	v_and_b32_e32 v136, 0xffff0000, v136
	v_and_b32_e32 v149, 0xffff0000, v134
	v_lshlrev_b32_e32 v134, 16, v137
	v_rcp_f32_e32 v147, v136
	v_rcp_f32_e32 v136, v134
	v_and_b32_e32 v134, 0xffff0000, v137
	v_rcp_f32_e32 v137, v134
	v_lshlrev_b32_e32 v134, 16, v135
	v_and_b32_e32 v135, 0xffff0000, v135
	v_rcp_f32_e32 v146, v143
	v_pk_mul_f32 v[134:135], v[136:137], v[134:135]
	v_pk_mul_f32 v[146:147], v[146:147], v[148:149]
	v_pk_mul_f32 v[100:101], v[100:101], v[134:135]
	v_or_b32_e32 v134, 32, v142
	v_ashrrev_i32_e32 v135, 31, v134
	v_lshlrev_b64 v[134:135], 14, v[134:135]
	v_lshl_add_u64 v[134:135], s[12:13], 0, v[134:135]
	v_lshl_add_u64 v[148:149], v[134:135], 0, v[144:145]
	v_pk_mul_f32 v[98:99], v[98:99], v[146:147]
	v_add_co_u32_e32 v146, vcc, s66, v148
	global_load_dwordx2 v[134:135], v[148:149], off nt
	s_nop 0
	v_addc_co_u32_e32 v147, vcc, 0, v149, vcc
	global_load_dwordx2 v[136:137], v[146:147], off nt
	s_waitcnt vmcnt(0)
	v_lshlrev_b32_e32 v154, 16, v134
	v_and_b32_e32 v155, 0xffff0000, v134
	v_lshlrev_b32_e32 v143, 16, v136
	v_and_b32_e32 v136, 0xffff0000, v136
	v_lshlrev_b32_e32 v134, 16, v137
	v_rcp_f32_e32 v153, v136
	v_rcp_f32_e32 v136, v134
	v_and_b32_e32 v134, 0xffff0000, v137
	v_rcp_f32_e32 v137, v134
	v_lshlrev_b32_e32 v134, 16, v135
	v_and_b32_e32 v135, 0xffff0000, v135
	v_rcp_f32_e32 v152, v143
	v_pk_mul_f32 v[134:135], v[136:137], v[134:135]
	v_pk_mul_f32 v[152:153], v[152:153], v[154:155]
	v_pk_mul_f32 v[96:97], v[96:97], v[134:135]
	global_load_dwordx2 v[134:135], v[148:149], off offset:32 nt
	global_load_dwordx2 v[136:137], v[146:147], off offset:32 nt
	v_pk_mul_f32 v[94:95], v[94:95], v[152:153]
	s_waitcnt vmcnt(0)
	v_lshlrev_b32_e32 v154, 16, v134
	v_lshlrev_b32_e32 v143, 16, v136
	v_and_b32_e32 v136, 0xffff0000, v136
	v_and_b32_e32 v155, 0xffff0000, v134
	v_lshlrev_b32_e32 v134, 16, v137
	v_rcp_f32_e32 v153, v136
	v_rcp_f32_e32 v136, v134
	v_and_b32_e32 v134, 0xffff0000, v137
	v_rcp_f32_e32 v137, v134
	v_lshlrev_b32_e32 v134, 16, v135
	v_and_b32_e32 v135, 0xffff0000, v135
	v_rcp_f32_e32 v152, v143
	v_pk_mul_f32 v[134:135], v[136:137], v[134:135]
	v_pk_mul_f32 v[152:153], v[152:153], v[154:155]
	v_pk_mul_f32 v[92:93], v[92:93], v[134:135]
	global_load_dwordx2 v[134:135], v[148:149], off offset:256 nt
	global_load_dwordx2 v[136:137], v[146:147], off offset:256 nt
	v_pk_mul_f32 v[90:91], v[90:91], v[152:153]
	s_waitcnt vmcnt(0)
	v_lshlrev_b32_e32 v154, 16, v134
	v_lshlrev_b32_e32 v143, 16, v136
	v_and_b32_e32 v136, 0xffff0000, v136
	v_and_b32_e32 v155, 0xffff0000, v134
	v_lshlrev_b32_e32 v134, 16, v137
	v_rcp_f32_e32 v153, v136
	v_rcp_f32_e32 v136, v134
	v_and_b32_e32 v134, 0xffff0000, v137
	v_rcp_f32_e32 v137, v134
	v_lshlrev_b32_e32 v134, 16, v135
	v_and_b32_e32 v135, 0xffff0000, v135
	v_rcp_f32_e32 v152, v143
	v_pk_mul_f32 v[134:135], v[136:137], v[134:135]
	v_pk_mul_f32 v[152:153], v[152:153], v[154:155]
	v_pk_mul_f32 v[88:89], v[88:89], v[134:135]
	global_load_dwordx2 v[134:135], v[148:149], off offset:288 nt
	global_load_dwordx2 v[136:137], v[146:147], off offset:288 nt
	v_pk_mul_f32 v[86:87], v[86:87], v[152:153]
	s_waitcnt vmcnt(0)
	v_lshlrev_b32_e32 v148, 16, v134
	v_lshlrev_b32_e32 v143, 16, v136
	v_and_b32_e32 v136, 0xffff0000, v136
	v_and_b32_e32 v149, 0xffff0000, v134
	v_lshlrev_b32_e32 v134, 16, v137
	v_rcp_f32_e32 v147, v136
	v_rcp_f32_e32 v136, v134
	v_and_b32_e32 v134, 0xffff0000, v137
	v_rcp_f32_e32 v137, v134
	v_lshlrev_b32_e32 v134, 16, v135
	v_and_b32_e32 v135, 0xffff0000, v135
	v_rcp_f32_e32 v146, v143
	v_pk_mul_f32 v[134:135], v[136:137], v[134:135]
	v_pk_mul_f32 v[146:147], v[146:147], v[148:149]
	v_pk_mul_f32 v[84:85], v[84:85], v[134:135]
	v_or_b32_e32 v134, 48, v142
	v_ashrrev_i32_e32 v135, 31, v134
	v_lshlrev_b64 v[134:135], 14, v[134:135]
	v_lshl_add_u64 v[134:135], s[12:13], 0, v[134:135]
	v_lshl_add_u64 v[144:145], v[134:135], 0, v[144:145]
	v_add_co_u32_e32 v142, vcc, s66, v144
	global_load_dwordx2 v[134:135], v[144:145], off nt
	s_nop 0
	v_addc_co_u32_e32 v143, vcc, 0, v145, vcc
	global_load_dwordx2 v[136:137], v[142:143], off nt
	v_pk_mul_f32 v[82:83], v[82:83], v[146:147]
	s_waitcnt vmcnt(0)
	v_lshlrev_b32_e32 v148, 16, v134
	v_and_b32_e32 v149, 0xffff0000, v134
	v_lshlrev_b32_e32 v146, 16, v136
	v_and_b32_e32 v136, 0xffff0000, v136
	v_lshlrev_b32_e32 v134, 16, v137
	v_rcp_f32_e32 v147, v136
	v_rcp_f32_e32 v136, v134
	v_and_b32_e32 v134, 0xffff0000, v137
	v_rcp_f32_e32 v137, v134
	v_lshlrev_b32_e32 v134, 16, v135
	v_and_b32_e32 v135, 0xffff0000, v135
	v_rcp_f32_e32 v146, v146
	v_pk_mul_f32 v[134:135], v[136:137], v[134:135]
	v_pk_mul_f32 v[146:147], v[146:147], v[148:149]
	v_pk_mul_f32 v[80:81], v[80:81], v[134:135]
	global_load_dwordx2 v[134:135], v[144:145], off offset:32 nt
	global_load_dwordx2 v[136:137], v[142:143], off offset:32 nt
	v_pk_mul_f32 v[78:79], v[78:79], v[146:147]
	s_waitcnt vmcnt(0)
; __device__ __forceinline__ int fresh_lane() { int l; asm volatile("v_mbcnt_lo_u32_b32 %0, -1, 0\n\tv_mbcnt_hi_u32_b32 %0, -1, %0" : "=v"(l)); return l; }
; __device__ __forceinline__ float bf_lo(unsigned w) { return __uint_as_float(w << 16); }
; __device__ __forceinline__ float bf_hi(unsigned w) { return __uint_as_float(w & 0xffff0000u); }
;     __device__ __forceinline__ void mid(f32x4 (&acc)[2][2][4][2], const Unit& u, int wr, int wc) const {
;         const int l_ = fresh_lane(), fr = l_ & 15, fq = l_ >> 4;
;         const int row0 = u.pm * BM + wr * 64 + fr, col0 = u.pn * BM + wc * 32 + 4 * fq;
; #pragma unroll
;         for (int ai = 0; ai < 2; ++ai)
; #pragma unroll
;             for (int m = 0; m < 4; ++m) { const size_t r = (size_t)(row0 + ai * HALF + m * 16);
; #pragma unroll
;                 for (int bj = 0; bj < 2; ++bj)
; #pragma unroll
;                     for (int n = 0; n < 2; ++n) { const u32x2 ga = *(const u32x2*)(G + r * ldg + col0 + bj * HALF + n * 16), gb = *(const u32x2*)(G + r * ldg + 4096 + col0 + bj * HALF + n * 16); f32x4 a = acc[ai][bj][m][n];
;                         a[0] *= bf_lo(ga.x) * __builtin_amdgcn_rcpf(bf_lo(gb.x)); a[1] *= bf_hi(ga.x) * __builtin_amdgcn_rcpf(bf_hi(gb.x)); a[2] *= bf_lo(ga.y) * __builtin_amdgcn_rcpf(bf_lo(gb.y)); a[3] *= bf_hi(ga.y) * __builtin_amdgcn_rcpf(bf_hi(gb.y));
;                         acc[ai][bj][m][n] = a; }
;                 asm volatile("" ::: "memory"); }
	v_lshlrev_b32_e32 v148, 16, v134
	v_lshlrev_b32_e32 v146, 16, v136
	v_and_b32_e32 v136, 0xffff0000, v136
	v_and_b32_e32 v149, 0xffff0000, v134
	v_lshlrev_b32_e32 v134, 16, v137
	v_rcp_f32_e32 v147, v136
	v_rcp_f32_e32 v136, v134
	v_and_b32_e32 v134, 0xffff0000, v137
	v_rcp_f32_e32 v137, v134
	v_lshlrev_b32_e32 v134, 16, v135
	v_and_b32_e32 v135, 0xffff0000, v135
	v_rcp_f32_e32 v146, v146
	v_pk_mul_f32 v[134:135], v[136:137], v[134:135]
	v_pk_mul_f32 v[146:147], v[146:147], v[148:149]
	v_pk_mul_f32 v[76:77], v[76:77], v[134:135]
	global_load_dwordx2 v[134:135], v[144:145], off offset:256 nt
	global_load_dwordx2 v[136:137], v[142:143], off offset:256 nt
	v_pk_mul_f32 v[74:75], v[74:75], v[146:147]
	s_waitcnt vmcnt(0)
	v_lshlrev_b32_e32 v148, 16, v134
	v_lshlrev_b32_e32 v146, 16, v136
	v_and_b32_e32 v136, 0xffff0000, v136
	v_and_b32_e32 v149, 0xffff0000, v134
	v_lshlrev_b32_e32 v134, 16, v137
	v_rcp_f32_e32 v147, v136
	v_rcp_f32_e32 v136, v134
	v_and_b32_e32 v134, 0xffff0000, v137
	v_rcp_f32_e32 v137, v134
	v_lshlrev_b32_e32 v134, 16, v135
	v_and_b32_e32 v135, 0xffff0000, v135
	v_rcp_f32_e32 v146, v146
	v_pk_mul_f32 v[134:135], v[136:137], v[134:135]
	v_pk_mul_f32 v[146:147], v[146:147], v[148:149]
	v_pk_mul_f32 v[72:73], v[72:73], v[134:135]
	global_load_dwordx2 v[134:135], v[144:145], off offset:288 nt
	global_load_dwordx2 v[136:137], v[142:143], off offset:288 nt
	v_pk_mul_f32 v[70:71], v[70:71], v[146:147]
	s_waitcnt vmcnt(0)
	v_lshlrev_b32_e32 v144, 16, v134
	v_lshlrev_b32_e32 v142, 16, v136
	v_and_b32_e32 v136, 0xffff0000, v136
	v_and_b32_e32 v145, 0xffff0000, v134
	v_lshlrev_b32_e32 v134, 16, v137
	v_rcp_f32_e32 v143, v136
	v_rcp_f32_e32 v136, v134
	v_and_b32_e32 v134, 0xffff0000, v137
	v_rcp_f32_e32 v142, v142
	v_rcp_f32_e32 v137, v134
	v_lshlrev_b32_e32 v134, 16, v135
	v_and_b32_e32 v135, 0xffff0000, v135
	v_pk_mul_f32 v[142:143], v[142:143], v[144:145]
	v_pk_mul_f32 v[134:135], v[136:137], v[134:135]
	v_lshl_add_u64 v[144:145], v[140:141], 0, s[54:55]
	s_mov_b32 s54, 0x200000
	v_pk_mul_f32 v[68:69], v[68:69], v[134:135]
	v_add_co_u32_e32 v134, vcc, s54, v140
	v_pk_mul_f32 v[66:67], v[66:67], v[142:143]
	s_nop 0
	v_addc_co_u32_e32 v135, vcc, 0, v141, vcc
	v_add_co_u32_e32 v142, vcc, s77, v140
	global_load_dwordx2 v[134:135], v[134:135], off nt
	s_nop 0
	v_addc_co_u32_e32 v143, vcc, 0, v141, vcc
	global_load_dwordx2 v[136:137], v[142:143], off nt
	s_waitcnt vmcnt(0)
	v_lshlrev_b32_e32 v148, 16, v134
	v_and_b32_e32 v149, 0xffff0000, v134
	v_lshlrev_b32_e32 v146, 16, v136
	v_and_b32_e32 v136, 0xffff0000, v136
	v_lshlrev_b32_e32 v134, 16, v137
	v_rcp_f32_e32 v147, v136
	v_rcp_f32_e32 v136, v134
	v_and_b32_e32 v134, 0xffff0000, v137
	v_rcp_f32_e32 v137, v134
	v_lshlrev_b32_e32 v134, 16, v135
	v_and_b32_e32 v135, 0xffff0000, v135
	v_rcp_f32_e32 v146, v146
	v_pk_mul_f32 v[134:135], v[136:137], v[134:135]
	v_pk_mul_f32 v[146:147], v[146:147], v[148:149]
	v_pk_mul_f32 v[64:65], v[64:65], v[134:135]
	global_load_dwordx2 v[134:135], v[144:145], off offset:32 nt
	global_load_dwordx2 v[136:137], v[142:143], off offset:32 nt
	v_pk_mul_f32 v[62:63], v[62:63], v[146:147]
	s_waitcnt vmcnt(0)
	v_lshlrev_b32_e32 v148, 16, v134
	v_lshlrev_b32_e32 v146, 16, v136
	v_and_b32_e32 v136, 0xffff0000, v136
	v_and_b32_e32 v149, 0xffff0000, v134
	v_lshlrev_b32_e32 v134, 16, v137
	v_rcp_f32_e32 v147, v136
	v_rcp_f32_e32 v136, v134
	v_and_b32_e32 v134, 0xffff0000, v137
	v_rcp_f32_e32 v137, v134
	v_lshlrev_b32_e32 v134, 16, v135
	v_and_b32_e32 v135, 0xffff0000, v135
	v_rcp_f32_e32 v146, v146
	v_pk_mul_f32 v[134:135], v[136:137], v[134:135]
	v_pk_mul_f32 v[146:147], v[146:147], v[148:149]
	v_pk_mul_f32 v[60:61], v[60:61], v[134:135]
	global_load_dwordx2 v[134:135], v[144:145], off offset:256 nt
	global_load_dwordx2 v[136:137], v[142:143], off offset:256 nt
	v_pk_mul_f32 v[58:59], v[58:59], v[146:147]
	s_waitcnt vmcnt(0)
	v_lshlrev_b32_e32 v148, 16, v134
	v_lshlrev_b32_e32 v146, 16, v136
	v_and_b32_e32 v136, 0xffff0000, v136
	v_and_b32_e32 v149, 0xffff0000, v134
	v_lshlrev_b32_e32 v134, 16, v137
	v_rcp_f32_e32 v147, v136
	v_rcp_f32_e32 v136, v134
	v_and_b32_e32 v134, 0xffff0000, v137
	v_rcp_f32_e32 v137, v134
	v_lshlrev_b32_e32 v134, 16, v135
	v_and_b32_e32 v135, 0xffff0000, v135
	v_rcp_f32_e32 v146, v146
	v_pk_mul_f32 v[134:135], v[136:137], v[134:135]
	v_pk_mul_f32 v[146:147], v[146:147], v[148:149]
	v_pk_mul_f32 v[56:57], v[56:57], v[134:135]
	global_load_dwordx2 v[134:135], v[144:145], off offset:288 nt
	global_load_dwordx2 v[136:137], v[142:143], off offset:288 nt
	v_pk_mul_f32 v[54:55], v[54:55], v[146:147]
	s_waitcnt vmcnt(0)
	v_lshlrev_b32_e32 v144, 16, v134
	v_lshlrev_b32_e32 v142, 16, v136
	v_and_b32_e32 v136, 0xffff0000, v136
	v_and_b32_e32 v145, 0xffff0000, v134
	v_lshlrev_b32_e32 v134, 16, v137
	v_rcp_f32_e32 v143, v136
	v_rcp_f32_e32 v136, v134
	v_and_b32_e32 v134, 0xffff0000, v137
	v_rcp_f32_e32 v137, v134
	v_rcp_f32_e32 v142, v142
	v_lshlrev_b32_e32 v134, 16, v135
	v_and_b32_e32 v135, 0xffff0000, v135
	v_pk_mul_f32 v[134:135], v[136:137], v[134:135]
	v_pk_mul_f32 v[142:143], v[142:143], v[144:145]
	v_pk_mul_f32 v[52:53], v[52:53], v[134:135]
	v_add_co_u32_e32 v134, vcc, s78, v140
	v_pk_mul_f32 v[50:51], v[50:51], v[142:143]
	s_nop 0
	v_addc_co_u32_e32 v135, vcc, 0, v141, vcc
	v_add_co_u32_e32 v142, vcc, s79, v140
	global_load_dwordx2 v[134:135], v[134:135], off nt
	s_nop 0
	v_addc_co_u32_e32 v143, vcc, 0, v141, vcc
	global_load_dwordx2 v[136:137], v[142:143], off nt
	v_lshl_add_u64 v[144:145], v[140:141], 0, s[30:31]
	s_waitcnt vmcnt(0)
; __device__ __forceinline__ float bf_lo(unsigned w) { return __uint_as_float(w << 16); }
; __device__ __forceinline__ float bf_hi(unsigned w) { return __uint_as_float(w & 0xffff0000u); }
;     __device__ __forceinline__ void mid(f32x4 (&acc)[2][2][4][2], const Unit& u, int wr, int wc) const {
;     ...
;                     for (int n = 0; n < 2; ++n) { const u32x2 ga = *(const u32x2*)(G + r * ldg + col0 + bj * HALF + n * 16), gb = *(const u32x2*)(G + r * ldg + 4096 + col0 + bj * HALF + n * 16); f32x4 a = acc[ai][bj][m][n];
;                         a[0] *= bf_lo(ga.x) * __builtin_amdgcn_rcpf(bf_lo(gb.x)); a[1] *= bf_hi(ga.x) * __builtin_amdgcn_rcpf(bf_hi(gb.x)); a[2] *= bf_lo(ga.y) * __builtin_amdgcn_rcpf(bf_lo(gb.y)); a[3] *= bf_hi(ga.y) * __builtin_amdgcn_rcpf(bf_hi(gb.y));
;                         acc[ai][bj][m][n] = a; }
	v_lshlrev_b32_e32 v148, 16, v134
	v_and_b32_e32 v149, 0xffff0000, v134
	v_lshlrev_b32_e32 v146, 16, v136
	v_and_b32_e32 v136, 0xffff0000, v136
	v_lshlrev_b32_e32 v134, 16, v137
	v_rcp_f32_e32 v147, v136
	v_rcp_f32_e32 v136, v134
	v_and_b32_e32 v134, 0xffff0000, v137
	v_rcp_f32_e32 v137, v134
	v_lshlrev_b32_e32 v134, 16, v135
	v_and_b32_e32 v135, 0xffff0000, v135
	v_rcp_f32_e32 v146, v146
	v_pk_mul_f32 v[134:135], v[136:137], v[134:135]
	v_pk_mul_f32 v[146:147], v[146:147], v[148:149]
	v_pk_mul_f32 v[48:49], v[48:49], v[134:135]
	global_load_dwordx2 v[134:135], v[144:145], off offset:32 nt
	global_load_dwordx2 v[136:137], v[142:143], off offset:32 nt
	v_pk_mul_f32 v[46:47], v[46:47], v[146:147]
	s_waitcnt vmcnt(0)
	v_lshlrev_b32_e32 v148, 16, v134
	v_lshlrev_b32_e32 v146, 16, v136
	v_and_b32_e32 v136, 0xffff0000, v136
	v_and_b32_e32 v149, 0xffff0000, v134
	v_lshlrev_b32_e32 v134, 16, v137
	v_rcp_f32_e32 v147, v136
	v_rcp_f32_e32 v136, v134
	v_and_b32_e32 v134, 0xffff0000, v137
	v_rcp_f32_e32 v137, v134
	v_lshlrev_b32_e32 v134, 16, v135
	v_and_b32_e32 v135, 0xffff0000, v135
	v_rcp_f32_e32 v146, v146
	v_pk_mul_f32 v[134:135], v[136:137], v[134:135]
	v_pk_mul_f32 v[146:147], v[146:147], v[148:149]
	v_pk_mul_f32 v[44:45], v[44:45], v[134:135]
	global_load_dwordx2 v[134:135], v[144:145], off offset:256 nt
	global_load_dwordx2 v[136:137], v[142:143], off offset:256 nt
	v_pk_mul_f32 v[42:43], v[42:43], v[146:147]
	s_waitcnt vmcnt(0)
	v_lshlrev_b32_e32 v148, 16, v134
	v_lshlrev_b32_e32 v146, 16, v136
	v_and_b32_e32 v136, 0xffff0000, v136
	v_and_b32_e32 v149, 0xffff0000, v134
	v_lshlrev_b32_e32 v134, 16, v137
	v_rcp_f32_e32 v147, v136
	v_rcp_f32_e32 v136, v134
	v_and_b32_e32 v134, 0xffff0000, v137
	v_rcp_f32_e32 v137, v134
	v_lshlrev_b32_e32 v134, 16, v135
	v_and_b32_e32 v135, 0xffff0000, v135
	v_rcp_f32_e32 v146, v146
	v_pk_mul_f32 v[134:135], v[136:137], v[134:135]
	v_pk_mul_f32 v[146:147], v[146:147], v[148:149]
	v_pk_mul_f32 v[40:41], v[40:41], v[134:135]
	global_load_dwordx2 v[134:135], v[144:145], off offset:288 nt
	global_load_dwordx2 v[136:137], v[142:143], off offset:288 nt
	v_pk_mul_f32 v[38:39], v[38:39], v[146:147]
	s_waitcnt vmcnt(0)
	v_lshlrev_b32_e32 v144, 16, v134
	v_lshlrev_b32_e32 v142, 16, v136
	v_and_b32_e32 v136, 0xffff0000, v136
	v_and_b32_e32 v145, 0xffff0000, v134
	v_lshlrev_b32_e32 v134, 16, v137
	v_rcp_f32_e32 v143, v136
	v_rcp_f32_e32 v136, v134
	v_and_b32_e32 v134, 0xffff0000, v137
	v_rcp_f32_e32 v137, v134
	v_rcp_f32_e32 v142, v142
	v_lshlrev_b32_e32 v134, 16, v135
	v_and_b32_e32 v135, 0xffff0000, v135
	v_pk_mul_f32 v[134:135], v[136:137], v[134:135]
	v_pk_mul_f32 v[142:143], v[142:143], v[144:145]
	v_pk_mul_f32 v[36:37], v[36:37], v[134:135]
	v_add_co_u32_e32 v134, vcc, s80, v140
	v_pk_mul_f32 v[34:35], v[34:35], v[142:143]
	s_nop 0
	v_addc_co_u32_e32 v135, vcc, 0, v141, vcc
	v_add_co_u32_e32 v142, vcc, s81, v140
	global_load_dwordx2 v[134:135], v[134:135], off nt
	s_nop 0
	v_addc_co_u32_e32 v143, vcc, 0, v141, vcc
	global_load_dwordx2 v[136:137], v[142:143], off nt
	v_lshl_add_u64 v[144:145], v[140:141], 0, s[38:39]
	s_waitcnt vmcnt(0)
	v_lshlrev_b32_e32 v148, 16, v134
	v_and_b32_e32 v149, 0xffff0000, v134
	v_lshlrev_b32_e32 v146, 16, v136
	v_and_b32_e32 v136, 0xffff0000, v136
	v_lshlrev_b32_e32 v134, 16, v137
	v_rcp_f32_e32 v147, v136
	v_rcp_f32_e32 v136, v134
	v_and_b32_e32 v134, 0xffff0000, v137
	v_rcp_f32_e32 v137, v134
	v_lshlrev_b32_e32 v134, 16, v135
	v_and_b32_e32 v135, 0xffff0000, v135
	v_rcp_f32_e32 v146, v146
	v_pk_mul_f32 v[134:135], v[136:137], v[134:135]
	v_pk_mul_f32 v[146:147], v[146:147], v[148:149]
	v_pk_mul_f32 v[32:33], v[32:33], v[134:135]
	global_load_dwordx2 v[134:135], v[144:145], off offset:32 nt
	global_load_dwordx2 v[136:137], v[142:143], off offset:32 nt
	v_pk_mul_f32 v[30:31], v[30:31], v[146:147]
	s_waitcnt vmcnt(0)
	v_lshlrev_b32_e32 v148, 16, v134
	v_lshlrev_b32_e32 v146, 16, v136
	v_and_b32_e32 v136, 0xffff0000, v136
	v_and_b32_e32 v149, 0xffff0000, v134
	v_lshlrev_b32_e32 v134, 16, v137
	v_rcp_f32_e32 v147, v136
	v_rcp_f32_e32 v136, v134
	v_and_b32_e32 v134, 0xffff0000, v137
	v_rcp_f32_e32 v137, v134
	v_lshlrev_b32_e32 v134, 16, v135
	v_and_b32_e32 v135, 0xffff0000, v135
	v_rcp_f32_e32 v146, v146
	v_pk_mul_f32 v[134:135], v[136:137], v[134:135]
	v_pk_mul_f32 v[146:147], v[146:147], v[148:149]
	v_pk_mul_f32 v[28:29], v[28:29], v[134:135]
	global_load_dwordx2 v[134:135], v[144:145], off offset:256 nt
	global_load_dwordx2 v[136:137], v[142:143], off offset:256 nt
	v_pk_mul_f32 v[26:27], v[26:27], v[146:147]
	s_waitcnt vmcnt(0)
; __device__ __forceinline__ float bf_lo(unsigned w) { return __uint_as_float(w << 16); }
; __device__ __forceinline__ float bf_hi(unsigned w) { return __uint_as_float(w & 0xffff0000u); }
;     __device__ __forceinline__ void mid(f32x4 (&acc)[2][2][4][2], const Unit& u, int wr, int wc) const {
;     ...
;                     for (int n = 0; n < 2; ++n) { const u32x2 ga = *(const u32x2*)(G + r * ldg + col0 + bj * HALF + n * 16), gb = *(const u32x2*)(G + r * ldg + 4096 + col0 + bj * HALF + n * 16); f32x4 a = acc[ai][bj][m][n];
;                         a[0] *= bf_lo(ga.x) * __builtin_amdgcn_rcpf(bf_lo(gb.x)); a[1] *= bf_hi(ga.x) * __builtin_amdgcn_rcpf(bf_hi(gb.x)); a[2] *= bf_lo(ga.y) * __builtin_amdgcn_rcpf(bf_lo(gb.y)); a[3] *= bf_hi(ga.y) * __builtin_amdgcn_rcpf(bf_hi(gb.y));
;                         acc[ai][bj][m][n] = a; }
;                 asm volatile("" ::: "memory"); }
	v_lshlrev_b32_e32 v148, 16, v134
	v_lshlrev_b32_e32 v146, 16, v136
	v_and_b32_e32 v136, 0xffff0000, v136
	v_and_b32_e32 v149, 0xffff0000, v134
	v_lshlrev_b32_e32 v134, 16, v137
	v_rcp_f32_e32 v147, v136
	v_rcp_f32_e32 v136, v134
	v_and_b32_e32 v134, 0xffff0000, v137
	v_rcp_f32_e32 v137, v134
	v_lshlrev_b32_e32 v134, 16, v135
	v_and_b32_e32 v135, 0xffff0000, v135
	v_rcp_f32_e32 v146, v146
	v_pk_mul_f32 v[134:135], v[136:137], v[134:135]
	v_pk_mul_f32 v[146:147], v[146:147], v[148:149]
	v_pk_mul_f32 v[24:25], v[24:25], v[134:135]
	global_load_dwordx2 v[134:135], v[144:145], off offset:288 nt
	global_load_dwordx2 v[136:137], v[142:143], off offset:288 nt
	v_pk_mul_f32 v[22:23], v[22:23], v[146:147]
	s_waitcnt vmcnt(0)
	v_lshlrev_b32_e32 v144, 16, v134
	v_lshlrev_b32_e32 v142, 16, v136
	v_and_b32_e32 v136, 0xffff0000, v136
	v_and_b32_e32 v145, 0xffff0000, v134
	v_lshlrev_b32_e32 v134, 16, v137
	v_rcp_f32_e32 v143, v136
	v_rcp_f32_e32 v136, v134
	v_and_b32_e32 v134, 0xffff0000, v137
	v_rcp_f32_e32 v137, v134
	v_rcp_f32_e32 v142, v142
	v_lshlrev_b32_e32 v134, 16, v135
	v_and_b32_e32 v135, 0xffff0000, v135
	v_pk_mul_f32 v[134:135], v[136:137], v[134:135]
	v_pk_mul_f32 v[142:143], v[142:143], v[144:145]
	v_pk_mul_f32 v[20:21], v[20:21], v[134:135]
	v_add_co_u32_e32 v134, vcc, s82, v140
	v_pk_mul_f32 v[18:19], v[18:19], v[142:143]
	s_nop 0
	v_addc_co_u32_e32 v135, vcc, 0, v141, vcc
	v_add_co_u32_e32 v142, vcc, s83, v140
	global_load_dwordx2 v[134:135], v[134:135], off nt
	s_nop 0
	v_addc_co_u32_e32 v143, vcc, 0, v141, vcc
	global_load_dwordx2 v[136:137], v[142:143], off nt
	v_lshl_add_u64 v[144:145], v[140:141], 0, s[40:41]
	s_waitcnt vmcnt(0)
	v_lshlrev_b32_e32 v146, 16, v134
	v_and_b32_e32 v147, 0xffff0000, v134
	v_lshlrev_b32_e32 v140, 16, v136
	v_and_b32_e32 v136, 0xffff0000, v136
	v_lshlrev_b32_e32 v134, 16, v137
	v_rcp_f32_e32 v141, v136
	v_rcp_f32_e32 v136, v134
	v_and_b32_e32 v134, 0xffff0000, v137
	v_rcp_f32_e32 v137, v134
	v_lshlrev_b32_e32 v134, 16, v135
	v_and_b32_e32 v135, 0xffff0000, v135
	v_rcp_f32_e32 v140, v140
	v_pk_mul_f32 v[134:135], v[136:137], v[134:135]
	v_pk_mul_f32 v[140:141], v[140:141], v[146:147]
	v_pk_mul_f32 v[16:17], v[16:17], v[134:135]
	global_load_dwordx2 v[134:135], v[144:145], off offset:32 nt
	global_load_dwordx2 v[136:137], v[142:143], off offset:32 nt
	v_pk_mul_f32 v[14:15], v[14:15], v[140:141]
	s_waitcnt vmcnt(0)
	v_lshlrev_b32_e32 v146, 16, v134
	v_lshlrev_b32_e32 v140, 16, v136
	v_and_b32_e32 v136, 0xffff0000, v136
	v_and_b32_e32 v147, 0xffff0000, v134
	v_lshlrev_b32_e32 v134, 16, v137
	v_rcp_f32_e32 v141, v136
	v_rcp_f32_e32 v136, v134
	v_and_b32_e32 v134, 0xffff0000, v137
	v_rcp_f32_e32 v137, v134
	v_lshlrev_b32_e32 v134, 16, v135
	v_and_b32_e32 v135, 0xffff0000, v135
	v_rcp_f32_e32 v140, v140
	v_pk_mul_f32 v[134:135], v[136:137], v[134:135]
	v_pk_mul_f32 v[140:141], v[140:141], v[146:147]
	v_pk_mul_f32 v[12:13], v[12:13], v[134:135]
	global_load_dwordx2 v[134:135], v[144:145], off offset:256 nt
	global_load_dwordx2 v[136:137], v[142:143], off offset:256 nt
	v_pk_mul_f32 v[10:11], v[10:11], v[140:141]
	s_waitcnt vmcnt(0)
	v_lshlrev_b32_e32 v146, 16, v134
	v_lshlrev_b32_e32 v140, 16, v136
	v_and_b32_e32 v136, 0xffff0000, v136
	v_rcp_f32_e32 v140, v140
	v_rcp_f32_e32 v141, v136
	v_and_b32_e32 v147, 0xffff0000, v134
	v_lshlrev_b32_e32 v134, 16, v137
	v_rcp_f32_e32 v136, v134
	v_pk_mul_f32 v[140:141], v[140:141], v[146:147]
	v_and_b32_e32 v134, 0xffff0000, v137
	v_pk_mul_f32 v[6:7], v[6:7], v[140:141]
	global_load_dwordx2 v[140:141], v[144:145], off offset:288 nt
	s_nop 0
	global_load_dwordx2 v[142:143], v[142:143], off offset:288 nt
	v_rcp_f32_e32 v137, v134
	v_lshlrev_b32_e32 v134, 16, v135
	v_and_b32_e32 v135, 0xffff0000, v135
	v_pk_mul_f32 v[134:135], v[136:137], v[134:135]
	s_waitcnt vmcnt(0)
	v_lshlrev_b32_e32 v136, 16, v140
	v_pk_mul_f32 v[8:9], v[8:9], v[134:135]
	v_lshlrev_b32_e32 v134, 16, v142
	v_and_b32_e32 v135, 0xffff0000, v142
	v_rcp_f32_e32 v134, v134
	v_rcp_f32_e32 v135, v135
	v_and_b32_e32 v137, 0xffff0000, v140
	v_pk_mul_f32 v[134:135], v[134:135], v[136:137]
	s_nop 0
	v_pk_mul_f32 v[2:3], v[2:3], v[134:135]
	v_lshlrev_b32_e32 v134, 16, v143
	v_and_b32_e32 v135, 0xffff0000, v143
	v_rcp_f32_e32 v134, v134
	v_rcp_f32_e32 v135, v135
	v_lshlrev_b32_e32 v136, 16, v141
	v_and_b32_e32 v137, 0xffff0000, v141
	v_pk_mul_f32 v[134:135], v[134:135], v[136:137]
	s_nop 0
	v_pk_mul_f32 v[4:5], v[4:5], v[134:135]
	s_branch .LBB0_2989

; __device__ __forceinline__ int fresh_lane() { int l; asm volatile("v_mbcnt_lo_u32_b32 %0, -1, 0\n\tv_mbcnt_hi_u32_b32 %0, -1, %0" : "=v"(l)); return l; }
; __device__ __forceinline__ float bf_lo(unsigned w) { return __uint_as_float(w << 16); }
; __device__ __forceinline__ float bf_hi(unsigned w) { return __uint_as_float(w & 0xffff0000u); }
;     __device__ __forceinline__ void operator()(const f32x4 (&acc)[2][2][4][2], const Unit& u, int wr, int wc, int fr_, int fq_) const {
;         const int l_ = fresh_lane(), fr = l_ & 15, fq = l_ >> 4;
;         const int row0 = u.pm * BM + wr * 64 + fr, col0 = u.pn * BM + wc * 32 + 4 * fq;
; #pragma unroll
;         for (int ai = 0; ai < 2; ++ai)
; #pragma unroll
;             for (int m = 0; m < 4; ++m) { const size_t r = (size_t)(row0 + ai * HALF + m * 16);
; #pragma unroll
;                 for (int bj = 0; bj < 2; ++bj)
; #pragma unroll
;                     for (int n = 0; n < 2; ++n) { const u32x2 g = *(const u32x2*)(G + r * ldg + 4096 + col0 + bj * HALF + n * 16); const f32x4 a = acc[ai][bj][m][n];
;                         int w8 = 0; w8 = __builtin_amdgcn_cvt_pk_fp8_f32(16.f * (a[0] * bf_lo(g.x)), 16.f * (a[1] * bf_hi(g.x)), w8, false); w8 = __builtin_amdgcn_cvt_pk_fp8_f32(16.f * (a[2] * bf_lo(g.y)), 16.f * (a[3] * bf_hi(g.y)), w8, true);
;                         *(int*)((unsigned char*)O + r * ldc + col0 + bj * HALF + n * 16) = w8; }
;                 asm volatile("" ::: "memory"); }
.LBB0_2994:
	v_mbcnt_lo_u32_b32 v134, -1, 0
	v_mbcnt_hi_u32_b32 v134, -1, v134
	s_add_i32 s87, s87, s74
	v_and_or_b32 v138, v134, 15, s87
	v_ashrrev_i32_e32 v134, 2, v134
	v_and_b32_e32 v134, -4, v134
	v_add_u32_e32 v134, s43, v134
	v_ashrrev_i32_e32 v139, 31, v138
	v_ashrrev_i32_e32 v135, 31, v134
	v_lshlrev_b64 v[136:137], 14, v[138:139]
	v_lshl_add_u64 v[136:137], s[12:13], 0, v[136:137]
	v_lshlrev_b64 v[140:141], 1, v[134:135]
	v_lshl_add_u64 v[136:137], v[136:137], 0, v[140:141]
	v_add_co_u32_e32 v136, vcc, s66, v136
	v_mov_b32_e32 v144, 0
	s_nop 0
	v_addc_co_u32_e32 v137, vcc, 0, v137, vcc
	global_load_dwordx2 v[142:143], v[136:137], off nt
	s_waitcnt vmcnt(0)
	v_lshlrev_b32_e32 v145, 16, v142
	v_and_b32_e32 v142, 0xffff0000, v142
	v_mul_f32_e32 v126, v126, v145
	v_mul_f32_e32 v127, v127, v142
	v_mul_f32_e32 v126, 0x41800000, v126
	v_mul_f32_e32 v127, 0x41800000, v127
	v_cvt_pk_fp8_f32 v144, v126, v127
	v_lshlrev_b32_e32 v146, 16, v143
	v_and_b32_e32 v143, 0xffff0000, v143
	v_mul_f32_e32 v128, v128, v146
	v_mul_f32_e32 v126, v129, v143
	v_mul_f32_e32 v127, 0x41800000, v128
	v_mul_f32_e32 v126, 0x41800000, v126
	v_cvt_pk_fp8_f32 v144, v127, v126 op_sel:[0,0,1]
	v_lshlrev_b64 v[128:129], 12, v[138:139]
	v_lshl_add_u64 v[126:127], s[14:15], 0, v[134:135]
	v_lshl_add_u64 v[128:129], v[126:127], 0, v[128:129]
	global_store_dword v[128:129], v144, off
	global_load_dwordx2 v[134:135], v[136:137], off offset:32 nt
	v_mov_b32_e32 v139, 0
	s_waitcnt vmcnt(0)
	v_lshlrev_b32_e32 v142, 16, v134
	v_and_b32_e32 v134, 0xffff0000, v134
	v_mul_f32_e32 v122, v122, v142
	v_mul_f32_e32 v123, v123, v134
	v_mul_f32_e32 v122, 0x41800000, v122
	v_mul_f32_e32 v123, 0x41800000, v123
	v_cvt_pk_fp8_f32 v139, v122, v123
	v_lshlrev_b32_e32 v143, 16, v135
	v_and_b32_e32 v135, 0xffff0000, v135
	v_mul_f32_e32 v124, v124, v143
	v_mul_f32_e32 v122, v125, v135
	v_mul_f32_e32 v123, 0x41800000, v124
	v_mul_f32_e32 v122, 0x41800000, v122
	v_cvt_pk_fp8_f32 v139, v123, v122 op_sel:[0,0,1]
	v_mov_b32_e32 v124, 0
	global_store_dword v[128:129], v139, off offset:16
	global_load_dwordx2 v[122:123], v[136:137], off offset:256 nt
	s_waitcnt vmcnt(0)
	v_lshlrev_b32_e32 v125, 16, v122
	v_and_b32_e32 v122, 0xffff0000, v122
	v_mul_f32_e32 v118, v118, v125
	v_mul_f32_e32 v119, v119, v122
	v_mul_f32_e32 v118, 0x41800000, v118
	v_mul_f32_e32 v119, 0x41800000, v119
	v_cvt_pk_fp8_f32 v124, v118, v119
	v_lshlrev_b32_e32 v134, 16, v123
	v_and_b32_e32 v123, 0xffff0000, v123
	v_mul_f32_e32 v120, v120, v134
	v_mul_f32_e32 v118, v121, v123
	v_mul_f32_e32 v119, 0x41800000, v120
	v_mul_f32_e32 v118, 0x41800000, v118
	v_cvt_pk_fp8_f32 v124, v119, v118 op_sel:[0,0,1]
	v_or_b32_e32 v120, 16, v138
	v_ashrrev_i32_e32 v121, 31, v120
	v_lshlrev_b64 v[122:123], 14, v[120:121]
	global_store_dword v[128:129], v124, off offset:128
	global_load_dwordx2 v[118:119], v[136:137], off offset:288 nt
	v_mov_b32_e32 v124, 0
	v_lshl_add_u64 v[122:123], s[12:13], 0, v[122:123]
	v_lshl_add_u64 v[122:123], v[122:123], 0, v[140:141]
	s_waitcnt vmcnt(0)
	v_lshlrev_b32_e32 v125, 16, v118
	v_and_b32_e32 v118, 0xffff0000, v118
	v_mul_f32_e32 v114, v114, v125
	v_mul_f32_e32 v115, v115, v118
	v_mul_f32_e32 v114, 0x41800000, v114
	v_mul_f32_e32 v115, 0x41800000, v115
	v_cvt_pk_fp8_f32 v124, v114, v115
	v_lshlrev_b32_e32 v134, 16, v119
	v_and_b32_e32 v119, 0xffff0000, v119
	v_mul_f32_e32 v116, v116, v134
	v_mul_f32_e32 v114, v117, v119
	v_mul_f32_e32 v115, 0x41800000, v116
	v_mul_f32_e32 v114, 0x41800000, v114
	v_cvt_pk_fp8_f32 v124, v115, v114 op_sel:[0,0,1]
	v_add_co_u32_e32 v114, vcc, s66, v122
	v_mov_b32_e32 v118, 0
	global_store_dword v[128:129], v124, off offset:144
	v_addc_co_u32_e32 v115, vcc, 0, v123, vcc
	global_load_dwordx2 v[116:117], v[114:115], off nt
	s_waitcnt vmcnt(0)
	v_lshlrev_b32_e32 v119, 16, v116
	v_and_b32_e32 v116, 0xffff0000, v116
	v_mul_f32_e32 v110, v110, v119
	v_mul_f32_e32 v111, v111, v116
	v_mul_f32_e32 v110, 0x41800000, v110
	v_mul_f32_e32 v111, 0x41800000, v111
	v_cvt_pk_fp8_f32 v118, v110, v111
	v_lshlrev_b32_e32 v122, 16, v117
	v_and_b32_e32 v117, 0xffff0000, v117
	v_mul_f32_e32 v112, v112, v122
	v_mul_f32_e32 v110, v113, v117
	v_mul_f32_e32 v111, 0x41800000, v112
	v_mul_f32_e32 v110, 0x41800000, v110
	v_cvt_pk_fp8_f32 v118, v111, v110 op_sel:[0,0,1]
	v_lshlrev_b64 v[110:111], 12, v[120:121]
	v_lshl_add_u64 v[110:111], v[126:127], 0, v[110:111]
	v_mov_b32_e32 v116, 0
	global_store_dword v[110:111], v118, off
	global_load_dwordx2 v[112:113], v[114:115], off offset:32 nt
	s_waitcnt vmcnt(0)
	v_lshlrev_b32_e32 v117, 16, v112
	v_and_b32_e32 v112, 0xffff0000, v112
	v_mul_f32_e32 v106, v106, v117
	v_mul_f32_e32 v107, v107, v112
	v_mul_f32_e32 v106, 0x41800000, v106
	v_mul_f32_e32 v107, 0x41800000, v107
	v_cvt_pk_fp8_f32 v116, v106, v107
	v_lshlrev_b32_e32 v118, 16, v113
	v_and_b32_e32 v113, 0xffff0000, v113
	v_mul_f32_e32 v108, v108, v118
	v_mul_f32_e32 v106, v109, v113
	v_mul_f32_e32 v107, 0x41800000, v108
	v_mul_f32_e32 v106, 0x41800000, v106
	v_cvt_pk_fp8_f32 v116, v107, v106 op_sel:[0,0,1]
	v_mov_b32_e32 v108, 0
	global_store_dword v[110:111], v116, off offset:16
	global_load_dwordx2 v[106:107], v[114:115], off offset:256 nt
	s_waitcnt vmcnt(0)
	v_lshlrev_b32_e32 v109, 16, v106
	v_and_b32_e32 v106, 0xffff0000, v106
	v_mul_f32_e32 v102, v102, v109
	v_mul_f32_e32 v103, v103, v106
	v_mul_f32_e32 v102, 0x41800000, v102
	v_mul_f32_e32 v103, 0x41800000, v103
	v_cvt_pk_fp8_f32 v108, v102, v103
	v_lshlrev_b32_e32 v112, 16, v107
	v_and_b32_e32 v107, 0xffff0000, v107
	v_mul_f32_e32 v104, v104, v112
	v_mul_f32_e32 v102, v105, v107
	v_mul_f32_e32 v103, 0x41800000, v104
	v_mul_f32_e32 v102, 0x41800000, v102
	v_cvt_pk_fp8_f32 v108, v103, v102 op_sel:[0,0,1]
	v_or_b32_e32 v104, 32, v138
	v_ashrrev_i32_e32 v105, 31, v104
	v_lshlrev_b64 v[106:107], 14, v[104:105]
	global_store_dword v[110:111], v108, off offset:128
	global_load_dwordx2 v[102:103], v[114:115], off offset:288 nt
	v_mov_b32_e32 v108, 0
	v_lshl_add_u64 v[106:107], s[12:13], 0, v[106:107]
	v_lshl_add_u64 v[106:107], v[106:107], 0, v[140:141]
	s_waitcnt vmcnt(0)
; __device__ __forceinline__ float bf_lo(unsigned w) { return __uint_as_float(w << 16); }
; __device__ __forceinline__ float bf_hi(unsigned w) { return __uint_as_float(w & 0xffff0000u); }
;     __device__ __forceinline__ void operator()(const f32x4 (&acc)[2][2][4][2], const Unit& u, int wr, int wc, int fr_, int fq_) const {
;     ...
;                     for (int n = 0; n < 2; ++n) { const u32x2 g = *(const u32x2*)(G + r * ldg + 4096 + col0 + bj * HALF + n * 16); const f32x4 a = acc[ai][bj][m][n];
;                         int w8 = 0; w8 = __builtin_amdgcn_cvt_pk_fp8_f32(16.f * (a[0] * bf_lo(g.x)), 16.f * (a[1] * bf_hi(g.x)), w8, false); w8 = __builtin_amdgcn_cvt_pk_fp8_f32(16.f * (a[2] * bf_lo(g.y)), 16.f * (a[3] * bf_hi(g.y)), w8, true);
;                         *(int*)((unsigned char*)O + r * ldc + col0 + bj * HALF + n * 16) = w8; }
;                 asm volatile("" ::: "memory"); }
	v_lshlrev_b32_e32 v109, 16, v102
	v_and_b32_e32 v102, 0xffff0000, v102
	v_mul_f32_e32 v98, v98, v109
	v_mul_f32_e32 v99, v99, v102
	v_mul_f32_e32 v98, 0x41800000, v98
	v_mul_f32_e32 v99, 0x41800000, v99
	v_cvt_pk_fp8_f32 v108, v98, v99
	v_lshlrev_b32_e32 v112, 16, v103
	v_and_b32_e32 v103, 0xffff0000, v103
	v_mul_f32_e32 v100, v100, v112
	v_mul_f32_e32 v98, v101, v103
	v_mul_f32_e32 v99, 0x41800000, v100
	v_mul_f32_e32 v98, 0x41800000, v98
	v_cvt_pk_fp8_f32 v108, v99, v98 op_sel:[0,0,1]
	v_add_co_u32_e32 v98, vcc, s66, v106
	v_mov_b32_e32 v102, 0
	global_store_dword v[110:111], v108, off offset:144
	v_addc_co_u32_e32 v99, vcc, 0, v107, vcc
	global_load_dwordx2 v[100:101], v[98:99], off nt
	s_waitcnt vmcnt(0)
	v_lshlrev_b32_e32 v103, 16, v100
	v_and_b32_e32 v100, 0xffff0000, v100
	v_mul_f32_e32 v94, v94, v103
	v_mul_f32_e32 v95, v95, v100
	v_mul_f32_e32 v94, 0x41800000, v94
	v_mul_f32_e32 v95, 0x41800000, v95
	v_cvt_pk_fp8_f32 v102, v94, v95
	v_lshlrev_b32_e32 v106, 16, v101
	v_and_b32_e32 v101, 0xffff0000, v101
	v_mul_f32_e32 v96, v96, v106
	v_mul_f32_e32 v94, v97, v101
	v_mul_f32_e32 v95, 0x41800000, v96
	v_mul_f32_e32 v94, 0x41800000, v94
	v_cvt_pk_fp8_f32 v102, v95, v94 op_sel:[0,0,1]
	v_lshlrev_b64 v[94:95], 12, v[104:105]
	v_lshl_add_u64 v[94:95], v[126:127], 0, v[94:95]
	v_mov_b32_e32 v100, 0
	global_store_dword v[94:95], v102, off
	global_load_dwordx2 v[96:97], v[98:99], off offset:32 nt
	s_waitcnt vmcnt(0)
	v_lshlrev_b32_e32 v101, 16, v96
	v_and_b32_e32 v96, 0xffff0000, v96
	v_mul_f32_e32 v90, v90, v101
	v_mul_f32_e32 v91, v91, v96
	v_mul_f32_e32 v90, 0x41800000, v90
	v_mul_f32_e32 v91, 0x41800000, v91
	v_cvt_pk_fp8_f32 v100, v90, v91
	v_lshlrev_b32_e32 v102, 16, v97
	v_and_b32_e32 v97, 0xffff0000, v97
	v_mul_f32_e32 v92, v92, v102
	v_mul_f32_e32 v90, v93, v97
	v_mul_f32_e32 v91, 0x41800000, v92
	v_mul_f32_e32 v90, 0x41800000, v90
	v_cvt_pk_fp8_f32 v100, v91, v90 op_sel:[0,0,1]
	v_mov_b32_e32 v92, 0
	global_store_dword v[94:95], v100, off offset:16
	global_load_dwordx2 v[90:91], v[98:99], off offset:256 nt
	s_waitcnt vmcnt(0)
	v_lshlrev_b32_e32 v93, 16, v90
	v_and_b32_e32 v90, 0xffff0000, v90
	v_mul_f32_e32 v86, v86, v93
	v_mul_f32_e32 v87, v87, v90
	v_mul_f32_e32 v86, 0x41800000, v86
	v_mul_f32_e32 v87, 0x41800000, v87
	v_cvt_pk_fp8_f32 v92, v86, v87
	v_lshlrev_b32_e32 v96, 16, v91
	v_and_b32_e32 v91, 0xffff0000, v91
	v_mul_f32_e32 v88, v88, v96
	v_mul_f32_e32 v86, v89, v91
	v_mul_f32_e32 v87, 0x41800000, v88
	v_mul_f32_e32 v86, 0x41800000, v86
	v_cvt_pk_fp8_f32 v92, v87, v86 op_sel:[0,0,1]
	v_or_b32_e32 v88, 48, v138
	v_ashrrev_i32_e32 v89, 31, v88
	v_lshlrev_b64 v[90:91], 14, v[88:89]
	global_store_dword v[94:95], v92, off offset:128
	global_load_dwordx2 v[86:87], v[98:99], off offset:288 nt
	v_mov_b32_e32 v92, 0
	v_lshl_add_u64 v[90:91], s[12:13], 0, v[90:91]
	v_lshl_add_u64 v[90:91], v[90:91], 0, v[140:141]
	s_waitcnt vmcnt(0)
	v_lshlrev_b32_e32 v93, 16, v86
	v_and_b32_e32 v86, 0xffff0000, v86
	v_mul_f32_e32 v82, v82, v93
	v_mul_f32_e32 v83, v83, v86
	v_mul_f32_e32 v82, 0x41800000, v82
	v_mul_f32_e32 v83, 0x41800000, v83
	v_cvt_pk_fp8_f32 v92, v82, v83
	v_lshlrev_b32_e32 v96, 16, v87
	v_and_b32_e32 v87, 0xffff0000, v87
	v_mul_f32_e32 v84, v84, v96
	v_mul_f32_e32 v82, v85, v87
	v_mul_f32_e32 v83, 0x41800000, v84
	v_mul_f32_e32 v82, 0x41800000, v82
	v_cvt_pk_fp8_f32 v92, v83, v82 op_sel:[0,0,1]
	v_add_co_u32_e32 v82, vcc, s66, v90
	v_mov_b32_e32 v86, 0
	global_store_dword v[94:95], v92, off offset:144
	v_addc_co_u32_e32 v83, vcc, 0, v91, vcc
	global_load_dwordx2 v[84:85], v[82:83], off nt
	s_waitcnt vmcnt(0)
	v_lshlrev_b32_e32 v87, 16, v84
	v_and_b32_e32 v84, 0xffff0000, v84
	v_mul_f32_e32 v78, v78, v87
	v_mul_f32_e32 v79, v79, v84
	v_mul_f32_e32 v78, 0x41800000, v78
	v_mul_f32_e32 v79, 0x41800000, v79
	v_cvt_pk_fp8_f32 v86, v78, v79
	v_lshlrev_b32_e32 v90, 16, v85
	v_and_b32_e32 v85, 0xffff0000, v85
	v_mul_f32_e32 v80, v80, v90
	v_mul_f32_e32 v78, v81, v85
	v_mul_f32_e32 v79, 0x41800000, v80
	v_mul_f32_e32 v78, 0x41800000, v78
	v_cvt_pk_fp8_f32 v86, v79, v78 op_sel:[0,0,1]
	v_lshlrev_b64 v[78:79], 12, v[88:89]
	v_lshl_add_u64 v[78:79], v[126:127], 0, v[78:79]
	v_mov_b32_e32 v84, 0
	global_store_dword v[78:79], v86, off
	global_load_dwordx2 v[80:81], v[82:83], off offset:32 nt
	s_waitcnt vmcnt(0)
	v_lshlrev_b32_e32 v85, 16, v80
	v_and_b32_e32 v80, 0xffff0000, v80
	v_mul_f32_e32 v74, v74, v85
	v_mul_f32_e32 v75, v75, v80
	v_mul_f32_e32 v74, 0x41800000, v74
	v_mul_f32_e32 v75, 0x41800000, v75
	v_cvt_pk_fp8_f32 v84, v74, v75
	v_lshlrev_b32_e32 v86, 16, v81
	v_and_b32_e32 v81, 0xffff0000, v81
	v_mul_f32_e32 v76, v76, v86
	v_mul_f32_e32 v74, v77, v81
	v_mul_f32_e32 v75, 0x41800000, v76
	v_mul_f32_e32 v74, 0x41800000, v74
	v_cvt_pk_fp8_f32 v84, v75, v74 op_sel:[0,0,1]
	v_mov_b32_e32 v76, 0
	global_store_dword v[78:79], v84, off offset:16
	global_load_dwordx2 v[74:75], v[82:83], off offset:256 nt
	s_waitcnt vmcnt(0)
	v_lshlrev_b32_e32 v77, 16, v74
	v_and_b32_e32 v74, 0xffff0000, v74
	v_mul_f32_e32 v70, v70, v77
	v_mul_f32_e32 v71, v71, v74
	v_mul_f32_e32 v70, 0x41800000, v70
	v_mul_f32_e32 v71, 0x41800000, v71
	v_cvt_pk_fp8_f32 v76, v70, v71
	v_lshlrev_b32_e32 v80, 16, v75
	v_and_b32_e32 v75, 0xffff0000, v75
	v_mul_f32_e32 v72, v72, v80
	v_mul_f32_e32 v70, v73, v75
	v_mul_f32_e32 v71, 0x41800000, v72
	v_mul_f32_e32 v70, 0x41800000, v70
	v_cvt_pk_fp8_f32 v76, v71, v70 op_sel:[0,0,1]
	v_add_u32_e32 v72, 0x80, v138
	v_ashrrev_i32_e32 v73, 31, v72
	v_lshlrev_b64 v[74:75], 14, v[72:73]
	global_store_dword v[78:79], v76, off offset:128
	global_load_dwordx2 v[70:71], v[82:83], off offset:288 nt
	v_mov_b32_e32 v76, 0
	v_lshl_add_u64 v[74:75], s[12:13], 0, v[74:75]
	v_lshl_add_u64 v[74:75], v[74:75], 0, v[140:141]
	s_waitcnt vmcnt(0)
; __device__ __forceinline__ float bf_lo(unsigned w) { return __uint_as_float(w << 16); }
; __device__ __forceinline__ float bf_hi(unsigned w) { return __uint_as_float(w & 0xffff0000u); }
;     __device__ __forceinline__ void operator()(const f32x4 (&acc)[2][2][4][2], const Unit& u, int wr, int wc, int fr_, int fq_) const {
;     ...
;                     for (int n = 0; n < 2; ++n) { const u32x2 g = *(const u32x2*)(G + r * ldg + 4096 + col0 + bj * HALF + n * 16); const f32x4 a = acc[ai][bj][m][n];
;                         int w8 = 0; w8 = __builtin_amdgcn_cvt_pk_fp8_f32(16.f * (a[0] * bf_lo(g.x)), 16.f * (a[1] * bf_hi(g.x)), w8, false); w8 = __builtin_amdgcn_cvt_pk_fp8_f32(16.f * (a[2] * bf_lo(g.y)), 16.f * (a[3] * bf_hi(g.y)), w8, true);
;                         *(int*)((unsigned char*)O + r * ldc + col0 + bj * HALF + n * 16) = w8; }
;                 asm volatile("" ::: "memory"); }
	v_lshlrev_b32_e32 v77, 16, v70
	v_and_b32_e32 v70, 0xffff0000, v70
	v_mul_f32_e32 v66, v66, v77
	v_mul_f32_e32 v67, v67, v70
	v_mul_f32_e32 v66, 0x41800000, v66
	v_mul_f32_e32 v67, 0x41800000, v67
	v_cvt_pk_fp8_f32 v76, v66, v67
	v_lshlrev_b32_e32 v80, 16, v71
	v_and_b32_e32 v71, 0xffff0000, v71
	v_mul_f32_e32 v68, v68, v80
	v_mul_f32_e32 v66, v69, v71
	v_mul_f32_e32 v67, 0x41800000, v68
	v_mul_f32_e32 v66, 0x41800000, v66
	v_cvt_pk_fp8_f32 v76, v67, v66 op_sel:[0,0,1]
	v_add_co_u32_e32 v66, vcc, s66, v74
	v_mov_b32_e32 v70, 0
	global_store_dword v[78:79], v76, off offset:144
	v_addc_co_u32_e32 v67, vcc, 0, v75, vcc
	global_load_dwordx2 v[68:69], v[66:67], off nt
	s_waitcnt vmcnt(0)
	v_lshlrev_b32_e32 v71, 16, v68
	v_and_b32_e32 v68, 0xffff0000, v68
	v_mul_f32_e32 v62, v62, v71
	v_mul_f32_e32 v63, v63, v68
	v_mul_f32_e32 v62, 0x41800000, v62
	v_mul_f32_e32 v63, 0x41800000, v63
	v_cvt_pk_fp8_f32 v70, v62, v63
	v_lshlrev_b32_e32 v74, 16, v69
	v_and_b32_e32 v69, 0xffff0000, v69
	v_mul_f32_e32 v64, v64, v74
	v_mul_f32_e32 v62, v65, v69
	v_mul_f32_e32 v63, 0x41800000, v64
	v_mul_f32_e32 v62, 0x41800000, v62
	v_cvt_pk_fp8_f32 v70, v63, v62 op_sel:[0,0,1]
	v_lshlrev_b64 v[62:63], 12, v[72:73]
	v_lshl_add_u64 v[62:63], v[126:127], 0, v[62:63]
	v_mov_b32_e32 v68, 0
	global_store_dword v[62:63], v70, off
	global_load_dwordx2 v[64:65], v[66:67], off offset:32 nt
	s_waitcnt vmcnt(0)
	v_lshlrev_b32_e32 v69, 16, v64
	v_and_b32_e32 v64, 0xffff0000, v64
	v_mul_f32_e32 v58, v58, v69
	v_mul_f32_e32 v59, v59, v64
	v_mul_f32_e32 v58, 0x41800000, v58
	v_mul_f32_e32 v59, 0x41800000, v59
	v_cvt_pk_fp8_f32 v68, v58, v59
	v_lshlrev_b32_e32 v70, 16, v65
	v_and_b32_e32 v65, 0xffff0000, v65
	v_mul_f32_e32 v60, v60, v70
	v_mul_f32_e32 v58, v61, v65
	v_mul_f32_e32 v59, 0x41800000, v60
	v_mul_f32_e32 v58, 0x41800000, v58
	v_cvt_pk_fp8_f32 v68, v59, v58 op_sel:[0,0,1]
	v_mov_b32_e32 v60, 0
	global_store_dword v[62:63], v68, off offset:16
	global_load_dwordx2 v[58:59], v[66:67], off offset:256 nt
	s_waitcnt vmcnt(0)
	v_lshlrev_b32_e32 v61, 16, v58
	v_and_b32_e32 v58, 0xffff0000, v58
	v_mul_f32_e32 v54, v54, v61
	v_mul_f32_e32 v55, v55, v58
	v_mul_f32_e32 v54, 0x41800000, v54
	v_mul_f32_e32 v55, 0x41800000, v55
	v_cvt_pk_fp8_f32 v60, v54, v55
	v_lshlrev_b32_e32 v64, 16, v59
	v_and_b32_e32 v59, 0xffff0000, v59
	v_mul_f32_e32 v56, v56, v64
	v_mul_f32_e32 v54, v57, v59
	v_mul_f32_e32 v55, 0x41800000, v56
	v_mul_f32_e32 v54, 0x41800000, v54
	v_cvt_pk_fp8_f32 v60, v55, v54 op_sel:[0,0,1]
	v_add_u32_e32 v56, 0x90, v138
	v_ashrrev_i32_e32 v57, 31, v56
	v_lshlrev_b64 v[58:59], 14, v[56:57]
	global_store_dword v[62:63], v60, off offset:128
	global_load_dwordx2 v[54:55], v[66:67], off offset:288 nt
	v_mov_b32_e32 v60, 0
	v_lshl_add_u64 v[58:59], s[12:13], 0, v[58:59]
	v_lshl_add_u64 v[58:59], v[58:59], 0, v[140:141]
	s_waitcnt vmcnt(0)
	v_lshlrev_b32_e32 v61, 16, v54
	v_and_b32_e32 v54, 0xffff0000, v54
	v_mul_f32_e32 v50, v50, v61
	v_mul_f32_e32 v51, v51, v54
	v_mul_f32_e32 v50, 0x41800000, v50
	v_mul_f32_e32 v51, 0x41800000, v51
	v_cvt_pk_fp8_f32 v60, v50, v51
	v_lshlrev_b32_e32 v64, 16, v55
	v_and_b32_e32 v55, 0xffff0000, v55
	v_mul_f32_e32 v52, v52, v64
	v_mul_f32_e32 v50, v53, v55
	v_mul_f32_e32 v51, 0x41800000, v52
	v_mul_f32_e32 v50, 0x41800000, v50
	v_cvt_pk_fp8_f32 v60, v51, v50 op_sel:[0,0,1]
	v_add_co_u32_e32 v50, vcc, s66, v58
	v_mov_b32_e32 v54, 0
	global_store_dword v[62:63], v60, off offset:144
	v_addc_co_u32_e32 v51, vcc, 0, v59, vcc
	global_load_dwordx2 v[52:53], v[50:51], off nt
	s_waitcnt vmcnt(0)
	v_lshlrev_b32_e32 v55, 16, v52
	v_and_b32_e32 v52, 0xffff0000, v52
	v_mul_f32_e32 v46, v46, v55
	v_mul_f32_e32 v47, v47, v52
	v_mul_f32_e32 v46, 0x41800000, v46
	v_mul_f32_e32 v47, 0x41800000, v47
	v_cvt_pk_fp8_f32 v54, v46, v47
	v_lshlrev_b32_e32 v58, 16, v53
	v_and_b32_e32 v53, 0xffff0000, v53
	v_mul_f32_e32 v48, v48, v58
	v_mul_f32_e32 v46, v49, v53
	v_mul_f32_e32 v47, 0x41800000, v48
	v_mul_f32_e32 v46, 0x41800000, v46
	v_cvt_pk_fp8_f32 v54, v47, v46 op_sel:[0,0,1]
	v_lshlrev_b64 v[46:47], 12, v[56:57]
	v_lshl_add_u64 v[46:47], v[126:127], 0, v[46:47]
	v_mov_b32_e32 v52, 0
	global_store_dword v[46:47], v54, off
	global_load_dwordx2 v[48:49], v[50:51], off offset:32 nt
	s_waitcnt vmcnt(0)
	v_lshlrev_b32_e32 v53, 16, v48
	v_and_b32_e32 v48, 0xffff0000, v48
	v_mul_f32_e32 v42, v42, v53
	v_mul_f32_e32 v43, v43, v48
	v_mul_f32_e32 v42, 0x41800000, v42
	v_mul_f32_e32 v43, 0x41800000, v43
	v_cvt_pk_fp8_f32 v52, v42, v43
	v_lshlrev_b32_e32 v54, 16, v49
	v_and_b32_e32 v49, 0xffff0000, v49
	v_mul_f32_e32 v44, v44, v54
	v_mul_f32_e32 v42, v45, v49
	v_mul_f32_e32 v43, 0x41800000, v44
	v_mul_f32_e32 v42, 0x41800000, v42
	v_cvt_pk_fp8_f32 v52, v43, v42 op_sel:[0,0,1]
	v_mov_b32_e32 v44, 0
	global_store_dword v[46:47], v52, off offset:16
	global_load_dwordx2 v[42:43], v[50:51], off offset:256 nt
	s_waitcnt vmcnt(0)
	v_lshlrev_b32_e32 v45, 16, v42
	v_and_b32_e32 v42, 0xffff0000, v42
	v_mul_f32_e32 v38, v38, v45
	v_mul_f32_e32 v39, v39, v42
	v_mul_f32_e32 v38, 0x41800000, v38
	v_mul_f32_e32 v39, 0x41800000, v39
	v_cvt_pk_fp8_f32 v44, v38, v39
	v_lshlrev_b32_e32 v48, 16, v43
	v_and_b32_e32 v43, 0xffff0000, v43
	v_mul_f32_e32 v40, v40, v48
	v_mul_f32_e32 v38, v41, v43
	v_mul_f32_e32 v39, 0x41800000, v40
	v_mul_f32_e32 v38, 0x41800000, v38
	v_cvt_pk_fp8_f32 v44, v39, v38 op_sel:[0,0,1]
	v_add_u32_e32 v40, 0xa0, v138
	v_ashrrev_i32_e32 v41, 31, v40
	v_lshlrev_b64 v[42:43], 14, v[40:41]
	global_store_dword v[46:47], v44, off offset:128
	global_load_dwordx2 v[38:39], v[50:51], off offset:288 nt
	v_mov_b32_e32 v44, 0
	v_lshl_add_u64 v[42:43], s[12:13], 0, v[42:43]
	v_lshl_add_u64 v[42:43], v[42:43], 0, v[140:141]
	s_waitcnt vmcnt(0)
; __device__ __forceinline__ float bf_lo(unsigned w) { return __uint_as_float(w << 16); }
; __device__ __forceinline__ float bf_hi(unsigned w) { return __uint_as_float(w & 0xffff0000u); }
; #define PG8_BAR __builtin_amdgcn_s_barrier()
;     __device__ __forceinline__ void operator()(const f32x4 (&acc)[2][2][4][2], const Unit& u, int wr, int wc, int fr_, int fq_) const {
;     ...
;                     for (int n = 0; n < 2; ++n) { const u32x2 g = *(const u32x2*)(G + r * ldg + 4096 + col0 + bj * HALF + n * 16); const f32x4 a = acc[ai][bj][m][n];
;                         int w8 = 0; w8 = __builtin_amdgcn_cvt_pk_fp8_f32(16.f * (a[0] * bf_lo(g.x)), 16.f * (a[1] * bf_hi(g.x)), w8, false); w8 = __builtin_amdgcn_cvt_pk_fp8_f32(16.f * (a[2] * bf_lo(g.y)), 16.f * (a[3] * bf_hi(g.y)), w8, true);
;                         *(int*)((unsigned char*)O + r * ldc + col0 + bj * HALF + n * 16) = w8; }
;                 asm volatile("" ::: "memory"); }
;     ...
;         if (!has_next) break;
; #pragma unroll
;         for (int a = 0; a < 2; ++a)
; #pragma unroll
;             for (int b = 0; b < 2; ++b)
; #pragma unroll
;                 for (int m = 0; m < 4; ++m)
; #pragma unroll
;                     for (int n = 0; n < 2; ++n) acc[a][b][m][n] = (f32x4){0.f, 0.f, 0.f, 0.f};
;         cur = nxt; cA = nA; cB = nB; ++ui;
;         if constexpr (ALIGN_EPI) { if (wr == 1) PG8_BAR; }
	v_lshlrev_b32_e32 v45, 16, v38
	v_and_b32_e32 v38, 0xffff0000, v38
	v_mul_f32_e32 v34, v34, v45
	v_mul_f32_e32 v35, v35, v38
	v_mul_f32_e32 v34, 0x41800000, v34
	v_mul_f32_e32 v35, 0x41800000, v35
	v_cvt_pk_fp8_f32 v44, v34, v35
	v_lshlrev_b32_e32 v48, 16, v39
	v_and_b32_e32 v39, 0xffff0000, v39
	v_mul_f32_e32 v36, v36, v48
	v_mul_f32_e32 v34, v37, v39
	v_mul_f32_e32 v35, 0x41800000, v36
	v_mul_f32_e32 v34, 0x41800000, v34
	v_cvt_pk_fp8_f32 v44, v35, v34 op_sel:[0,0,1]
	v_add_co_u32_e32 v34, vcc, s66, v42
	v_mov_b32_e32 v38, 0
	global_store_dword v[46:47], v44, off offset:144
	v_addc_co_u32_e32 v35, vcc, 0, v43, vcc
	global_load_dwordx2 v[36:37], v[34:35], off nt
	s_waitcnt vmcnt(0)
	v_lshlrev_b32_e32 v39, 16, v36
	v_and_b32_e32 v36, 0xffff0000, v36
	v_mul_f32_e32 v30, v30, v39
	v_mul_f32_e32 v31, v31, v36
	v_mul_f32_e32 v30, 0x41800000, v30
	v_mul_f32_e32 v31, 0x41800000, v31
	v_cvt_pk_fp8_f32 v38, v30, v31
	v_lshlrev_b32_e32 v42, 16, v37
	v_and_b32_e32 v37, 0xffff0000, v37
	v_mul_f32_e32 v32, v32, v42
	v_mul_f32_e32 v30, v33, v37
	v_mul_f32_e32 v31, 0x41800000, v32
	v_mul_f32_e32 v30, 0x41800000, v30
	v_cvt_pk_fp8_f32 v38, v31, v30 op_sel:[0,0,1]
	v_lshlrev_b64 v[30:31], 12, v[40:41]
	v_lshl_add_u64 v[30:31], v[126:127], 0, v[30:31]
	v_mov_b32_e32 v36, 0
	global_store_dword v[30:31], v38, off
	global_load_dwordx2 v[32:33], v[34:35], off offset:32 nt
	s_waitcnt vmcnt(0)
	v_lshlrev_b32_e32 v37, 16, v32
	v_and_b32_e32 v32, 0xffff0000, v32
	v_mul_f32_e32 v26, v26, v37
	v_mul_f32_e32 v27, v27, v32
	v_mul_f32_e32 v26, 0x41800000, v26
	v_mul_f32_e32 v27, 0x41800000, v27
	v_cvt_pk_fp8_f32 v36, v26, v27
	v_lshlrev_b32_e32 v38, 16, v33
	v_and_b32_e32 v33, 0xffff0000, v33
	v_mul_f32_e32 v28, v28, v38
	v_mul_f32_e32 v26, v29, v33
	v_mul_f32_e32 v27, 0x41800000, v28
	v_mul_f32_e32 v26, 0x41800000, v26
	v_cvt_pk_fp8_f32 v36, v27, v26 op_sel:[0,0,1]
	v_mov_b32_e32 v28, 0
	global_store_dword v[30:31], v36, off offset:16
	global_load_dwordx2 v[26:27], v[34:35], off offset:256 nt
	s_waitcnt vmcnt(0)
	v_lshlrev_b32_e32 v29, 16, v26
	v_and_b32_e32 v26, 0xffff0000, v26
	v_mul_f32_e32 v22, v22, v29
	v_mul_f32_e32 v23, v23, v26
	v_mul_f32_e32 v22, 0x41800000, v22
	v_mul_f32_e32 v23, 0x41800000, v23
	v_cvt_pk_fp8_f32 v28, v22, v23
	v_lshlrev_b32_e32 v32, 16, v27
	v_and_b32_e32 v27, 0xffff0000, v27
	v_mul_f32_e32 v24, v24, v32
	v_mul_f32_e32 v22, v25, v27
	v_mul_f32_e32 v23, 0x41800000, v24
	v_mul_f32_e32 v22, 0x41800000, v22
	v_cvt_pk_fp8_f32 v28, v23, v22 op_sel:[0,0,1]
	v_add_u32_e32 v24, 0xb0, v138
	v_ashrrev_i32_e32 v25, 31, v24
	v_lshlrev_b64 v[26:27], 14, v[24:25]
	global_store_dword v[30:31], v28, off offset:128
	global_load_dwordx2 v[22:23], v[34:35], off offset:288 nt
	v_mov_b32_e32 v28, 0
	v_lshl_add_u64 v[26:27], s[12:13], 0, v[26:27]
	v_lshl_add_u64 v[26:27], v[26:27], 0, v[140:141]
	s_waitcnt vmcnt(0)
	v_lshlrev_b32_e32 v29, 16, v22
	v_and_b32_e32 v22, 0xffff0000, v22
	v_mul_f32_e32 v18, v18, v29
	v_mul_f32_e32 v19, v19, v22
	v_mul_f32_e32 v18, 0x41800000, v18
	v_mul_f32_e32 v19, 0x41800000, v19
	v_cvt_pk_fp8_f32 v28, v18, v19
	v_lshlrev_b32_e32 v32, 16, v23
	v_and_b32_e32 v23, 0xffff0000, v23
	v_mul_f32_e32 v20, v20, v32
	v_mul_f32_e32 v18, v21, v23
	v_mul_f32_e32 v19, 0x41800000, v20
	v_mul_f32_e32 v18, 0x41800000, v18
	v_cvt_pk_fp8_f32 v28, v19, v18 op_sel:[0,0,1]
	v_add_co_u32_e32 v18, vcc, s66, v26
	v_mov_b32_e32 v22, 0
	global_store_dword v[30:31], v28, off offset:144
	v_addc_co_u32_e32 v19, vcc, 0, v27, vcc
	global_load_dwordx2 v[20:21], v[18:19], off nt
	s_andn2_b64 vcc, exec, s[0:1]
	s_mov_b64 s[0:1], -1
	s_waitcnt vmcnt(0)
	v_lshlrev_b32_e32 v23, 16, v20
	v_and_b32_e32 v20, 0xffff0000, v20
	v_mul_f32_e32 v14, v14, v23
	v_mul_f32_e32 v15, v15, v20
	v_mul_f32_e32 v14, 0x41800000, v14
	v_mul_f32_e32 v15, 0x41800000, v15
	v_cvt_pk_fp8_f32 v22, v14, v15
	v_lshlrev_b32_e32 v26, 16, v21
	v_and_b32_e32 v21, 0xffff0000, v21
	v_mul_f32_e32 v16, v16, v26
	v_mul_f32_e32 v14, v17, v21
	v_mul_f32_e32 v15, 0x41800000, v16
	v_mul_f32_e32 v14, 0x41800000, v14
	v_cvt_pk_fp8_f32 v22, v15, v14 op_sel:[0,0,1]
	v_lshlrev_b64 v[14:15], 12, v[24:25]
	v_lshl_add_u64 v[14:15], v[126:127], 0, v[14:15]
	v_mov_b32_e32 v20, 0
	global_store_dword v[14:15], v22, off
	global_load_dwordx2 v[16:17], v[18:19], off offset:32 nt
	s_waitcnt vmcnt(0)
	v_lshlrev_b32_e32 v21, 16, v16
	v_and_b32_e32 v16, 0xffff0000, v16
	v_mul_f32_e32 v10, v10, v21
	v_mul_f32_e32 v11, v11, v16
	v_mul_f32_e32 v10, 0x41800000, v10
	v_mul_f32_e32 v11, 0x41800000, v11
	v_cvt_pk_fp8_f32 v20, v10, v11
	v_lshlrev_b32_e32 v22, 16, v17
	v_and_b32_e32 v17, 0xffff0000, v17
	v_mul_f32_e32 v12, v12, v22
	v_mul_f32_e32 v10, v13, v17
	v_mul_f32_e32 v11, 0x41800000, v12
	v_mul_f32_e32 v10, 0x41800000, v10
	v_cvt_pk_fp8_f32 v20, v11, v10 op_sel:[0,0,1]
	v_mov_b32_e32 v12, 0
	global_store_dword v[14:15], v20, off offset:16
	global_load_dwordx2 v[10:11], v[18:19], off offset:256 nt
	s_waitcnt vmcnt(0)
	v_lshlrev_b32_e32 v13, 16, v10
	v_and_b32_e32 v10, 0xffff0000, v10
	v_mul_f32_e32 v6, v6, v13
	v_mul_f32_e32 v7, v7, v10
	v_mul_f32_e32 v6, 0x41800000, v6
	v_mul_f32_e32 v7, 0x41800000, v7
	v_cvt_pk_fp8_f32 v12, v6, v7
	v_lshlrev_b32_e32 v16, 16, v11
	v_and_b32_e32 v11, 0xffff0000, v11
	v_mul_f32_e32 v8, v8, v16
	v_mul_f32_e32 v6, v9, v11
	v_mul_f32_e32 v7, 0x41800000, v8
	v_mul_f32_e32 v6, 0x41800000, v6
	v_cvt_pk_fp8_f32 v12, v7, v6 op_sel:[0,0,1]
	v_mov_b32_e32 v8, 0
	global_store_dword v[14:15], v12, off offset:128
	global_load_dwordx2 v[6:7], v[18:19], off offset:288 nt
	s_waitcnt vmcnt(0)
	v_lshlrev_b32_e32 v9, 16, v6
	v_and_b32_e32 v6, 0xffff0000, v6
	v_mul_f32_e32 v2, v2, v9
	v_mul_f32_e32 v3, v3, v6
	v_mul_f32_e32 v2, 0x41800000, v2
	v_mul_f32_e32 v3, 0x41800000, v3
	v_cvt_pk_fp8_f32 v8, v2, v3
	v_lshlrev_b32_e32 v10, 16, v7
	v_and_b32_e32 v7, 0xffff0000, v7
	v_mul_f32_e32 v4, v4, v10
	v_mul_f32_e32 v2, v5, v7
	v_mul_f32_e32 v3, 0x41800000, v4
	v_mul_f32_e32 v2, 0x41800000, v2
	v_cvt_pk_fp8_f32 v8, v3, v2 op_sel:[0,0,1]
	global_store_dword v[14:15], v8, off offset:144
	s_cbranch_vccnz .LBB0_2981
	s_andn2_b64 vcc, exec, s[10:11]
	s_cbranch_vccnz .LBB0_2980
	s_barrier
	s_branch .LBB0_2980
